# selection pass 2 and take loops: lane ranks via v_mbcnt, ballots moved with SALU (on top of the bin-edge and pass-1 rewrites)
# speedup vs baseline: 1.0177x; 1.0054x over previous
; __device__ __forceinline__ bool dsa2_sampled(LAS unsigned char* wl, const unsigned (&kk)[128], int nreg, int n, int lane) {
;     ...
;     for (int s = 0; s < mxc; ++s) { const bool vld = s < cur; const unsigned long long e = vld ? PRIV[s * 64 + lane] : 0ull; const unsigned k = (unsigned)(e >> 32), ix = (unsigned)e;
;         const bool sure = vld && (k >> 21) > bh, cand = vld && !sure;
;         const unsigned long long ms = __ballot(sure), mc = __ballot(cand);
;         const int ps = A + __builtin_popcountll(ms & ltm), pc = C + __builtin_popcountll(mc & ltm);
;         if (sure && ps < 256) LIST[ps] = (int)ix;
;         if (cand) PRIV[pc] = ((unsigned long long)k << 13) | (unsigned long long)(8191u - ix);
;         A += __builtin_popcountll(ms); C += __builtin_popcountll(mc); }
.LBB0_1231:
	s_waitcnt lgkmcnt(0)
	v_mov_b64_e32 v[0:1], v[186:187]
	ds_read_b64 v[186:187], v4 offset:512
	v_cmp_lt_u32_e64 s[0:1], s13, v3
	v_lshrrev_b32_e32 v5, 21, v1
	v_cmp_lt_u32_e32 vcc, v2, v5
	s_and_b64 vcc, s[0:1], vcc
	s_andn2_b64 s[0:1], s[0:1], vcc
	v_mbcnt_lo_u32_b32 v5, vcc_lo, 0
	v_mbcnt_hi_u32_b32 v5, vcc_hi, v5
	v_add_u32_e32 v5, s20, v5
	v_cmp_gt_u32_e64 s[2:3], s90, v5
	s_and_b64 s[14:15], vcc, s[2:3]
	s_and_saveexec_b64 s[2:3], s[14:15]
	v_lshl_add_u32 v5, v5, 2, s57
	ds_write_b32 v5, v0 offset:12288
	s_or_b64 exec, exec, s[2:3]
	s_and_saveexec_b64 s[2:3], s[0:1]
	s_cbranch_execz .LBB0_1230
	v_mbcnt_lo_u32_b32 v5, s0, 0
	v_lshrrev_b64 v[8:9], 19, v[0:1]
	v_sub_u32_e32 v0, 0x1fff, v0
	s_movk_i32 s4, 0xe000
	v_mbcnt_hi_u32_b32 v5, s1, v5
	v_and_or_b32 v8, v8, s4, v0
	s_lshl_b32 s4, s21, 3
	s_add_i32 s4, s57, s4
	v_lshl_add_u32 v0, v5, 3, s4
	ds_write_b64 v0, v[8:9]
	s_branch .LBB0_1230

; __device__ __forceinline__ bool dsa2_sampled(LAS unsigned char* wl, const unsigned (&kk)[128], int nreg, int n, int lane) {
;     ...
;         for (int it = 0; it < nit; ++it) { const int i = it * 64 + lane; unsigned long long c2 = 0ull; if (i < C) c2 = PRIV[i];
;             const bool take = (i < C) && ((c2 >> shf) >= prefix);
;             const unsigned long long mt = __ballot(take);
;             if (take) LIST[pos + __builtin_popcountll(mt & ltm)] = (int)(8191u - (unsigned)(c2 & 8191ull));
;             pos += __builtin_popcountll(mt); }
.LBB0_1266:
	s_waitcnt lgkmcnt(0)
	v_mov_b64_e32 v[2:3], v[184:185]
	ds_read_b64 v[184:185], v6 offset:512
	v_cmp_gt_u32_e32 vcc, s21, v1
	v_lshrrev_b64 v[8:9], v0, v[2:3]
	v_cmp_ge_u64_e64 s[0:1], v[8:9], v[4:5]
	s_and_b64 vcc, vcc, s[0:1]
	s_and_saveexec_b64 s[0:1], vcc
	s_cbranch_execz .LBB0_1265
	v_mbcnt_lo_u32_b32 v3, vcc_lo, 0
	s_lshl_b32 s2, s20, 2
	s_add_i32 s2, s57, s2
	v_mbcnt_hi_u32_b32 v3, vcc_hi, v3
	v_lshl_add_u32 v3, v3, 2, s2
	s_movk_i32 s2, 0x1fff
	v_bitop3_b32 v2, v2, s2, v2 bitop3:0xc
	ds_write_b32 v3, v2 offset:12288
	s_branch .LBB0_1265
